# v39: v37 + nt (streaming) on the 32 single-use residual-row loads of the out-proj epilogue
# speedup vs baseline: 1.0077x; 1.0077x over previous
; #define GAS __attribute__((address_space(1)))
;     __device__ __forceinline__ void operator()(const f32x4 (&acc)[2][2][4][2], const Unit& u, int wr, int wc, int fr, int fq) const {
;         const int row0 = u.pm * 256 + wr * 64 + fr, col0 = u.pn * 256 + wc * 32 + 4 * fq; const float* gp = gate + (u.pm >> 3) * MODW + col0;
;         f32x4 gv[2][2];
; #pragma unroll
;         for (int bj = 0; bj < 2; ++bj)
; #pragma unroll
;             for (int n = 0; n < 2; ++n) gv[bj][n] = *(const GAS f32x4*)(gp + bj * 128 + n * 16) * scale;
;         size_t off0 = (size_t)row0 * DM + col0; asm volatile("" : "+v"(off0));
;         f32x4 B0[4], B1[4];
;     ...
;         ER_LOAD(B0, 0); ER_LOAD(B1, 1); ER_STORE(B0, 0); ER_LOAD(B0, 2); ER_STORE(B1, 1); ER_LOAD(B1, 3); ER_STORE(B0, 2); ER_LOAD(B0, 4); ER_STORE(B1, 3); ER_LOAD(B1, 5);
.LBB0_2085:
	s_lshr_b32 s23, s30, 3
	s_mul_i32 s34, s23, 0x6000
	s_ashr_i32 s35, s34, 31
	s_lshl_b64 s[34:35], s[34:35], 2
	v_lshl_or_b32 v6, s31, 8, v183
	s_add_u32 s34, s49, s34
	s_addc_u32 s35, s50, s35
	v_ashrrev_i32_e32 v7, 31, v6
	s_nop 15
	s_nop 15
	v_lshl_add_u64 v[8:9], v[6:7], 2, s[34:35]
	global_load_dwordx4 v[2:5], v[8:9], off
	global_load_dwordx4 v[236:239], v[8:9], off offset:64
	global_load_dwordx4 v[240:243], v[8:9], off offset:512
	global_load_dwordx4 v[244:247], v[8:9], off offset:576
	v_readlane_b32 s60, v249, 15
	v_readlane_b32 s61, v249, 16
	s_mov_b32 s23, 0x80000
	v_readlane_b32 s62, v249, 17
	v_readlane_b32 s63, v249, 18
	v_readlane_b32 s64, v249, 19
	v_readlane_b32 s65, v249, 20
	v_readlane_b32 s66, v249, 21
	v_readlane_b32 s67, v249, 22
	v_readlane_b32 s68, v249, 23
	v_readlane_b32 s69, v249, 24
	v_readlane_b32 s70, v249, 25
	v_readlane_b32 s71, v249, 26
	v_readlane_b32 s72, v249, 27
	v_readlane_b32 s73, v249, 28
	v_readlane_b32 s74, v249, 29
	v_readlane_b32 s75, v249, 30
	s_waitcnt vmcnt(0)
	v_pk_mul_f32 v[30:31], v[4:5], s[18:19] op_sel_hi:[1,0]
	v_pk_mul_f32 v[32:33], v[2:3], s[18:19] op_sel_hi:[1,0]
	v_pk_mul_f32 v[18:19], v[238:239], s[18:19] op_sel_hi:[1,0]
	v_pk_mul_f32 v[20:21], v[236:237], s[18:19] op_sel_hi:[1,0]
	v_pk_mul_f32 v[22:23], v[242:243], s[18:19] op_sel_hi:[1,0]
	v_pk_mul_f32 v[24:25], v[240:241], s[18:19] op_sel_hi:[1,0]
	v_pk_mul_f32 v[28:29], v[244:245], s[18:19] op_sel_hi:[1,0]
	v_lshl_add_u32 v2, s30, 8, v1
	v_ashrrev_i32_e32 v3, 31, v2
	v_lshlrev_b64 v[2:3], 12, v[2:3]
	v_lshl_add_u64 v[188:189], v[2:3], 0, v[6:7]
	v_pk_mul_f32 v[26:27], v[246:247], s[18:19] op_sel_hi:[1,0]
	v_lshl_add_u64 v[174:175], v[188:189], 2, s[60:61]
	global_load_dwordx4 v[2:5], v[174:175], off nt
	global_load_dwordx4 v[6:9], v[174:175], off offset:64 nt
	global_load_dwordx4 v[10:13], v[174:175], off offset:512 nt
	global_load_dwordx4 v[14:17], v[174:175], off offset:576 nt
	v_add_co_u32_e32 v176, vcc, s57, v174
	v_lshl_add_u64 v[200:201], v[174:175], 0, s[20:21]
	s_nop 0
	v_addc_co_u32_e32 v177, vcc, 0, v175, vcc
	global_load_dwordx4 v[176:179], v[176:177], off nt
	s_nop 0
	global_load_dwordx4 v[192:195], v[200:201], off offset:64 nt
	global_load_dwordx4 v[196:199], v[200:201], off offset:512 nt
	s_nop 0
	global_load_dwordx4 v[200:203], v[200:201], off offset:576 nt
	v_readlane_b32 s30, v248, 6
	v_readlane_b32 s31, v248, 7
	s_waitcnt vmcnt(7)
	v_pk_fma_f32 v[4:5], v[160:161], v[30:31], v[4:5]
	v_pk_fma_f32 v[2:3], v[158:159], v[32:33], v[2:3]
	v_lshl_add_u64 v[158:159], v[188:189], 1, s[30:31]
	v_cvt_pk_bf16_f32 v2, v2, v3
	v_cvt_pk_bf16_f32 v3, v4, v5
	s_waitcnt vmcnt(6)
	v_pk_fma_f32 v[4:5], v[154:155], v[20:21], v[6:7]
	global_store_dwordx2 v[158:159], v[2:3], off
	v_pk_fma_f32 v[2:3], v[156:157], v[18:19], v[8:9]
	v_cvt_pk_bf16_f32 v4, v4, v5
	s_mov_b64 s[30:31], 0x80000
	v_cvt_pk_bf16_f32 v5, v2, v3
	global_store_dwordx2 v[158:159], v[4:5], off offset:32
	s_waitcnt vmcnt(7)
	v_pk_fma_f32 v[4:5], v[150:151], v[24:25], v[10:11]
	v_pk_fma_f32 v[2:3], v[152:153], v[22:23], v[12:13]
	v_cvt_pk_bf16_f32 v4, v4, v5
	s_waitcnt vmcnt(5)
	v_pk_fma_f32 v[144:145], v[144:145], v[30:31], v[178:179]
	v_cvt_pk_bf16_f32 v5, v2, v3
	global_store_dwordx2 v[158:159], v[4:5], off offset:256
	v_pk_fma_f32 v[4:5], v[146:147], v[28:29], v[14:15]
	v_pk_fma_f32 v[2:3], v[148:149], v[26:27], v[16:17]
	v_cvt_pk_bf16_f32 v4, v4, v5
	v_pk_fma_f32 v[142:143], v[142:143], v[32:33], v[176:177]
	v_cvt_pk_bf16_f32 v5, v2, v3
	global_store_dwordx2 v[158:159], v[4:5], off offset:288
	v_add_co_u32_e32 v4, vcc, s23, v174
	v_lshl_add_u64 v[2:3], v[174:175], 0, s[30:31]
	s_nop 0
	v_addc_co_u32_e32 v5, vcc, 0, v175, vcc
	global_load_dwordx4 v[14:17], v[4:5], off nt
	global_load_dwordx4 v[10:13], v[2:3], off offset:64 nt
	global_load_dwordx4 v[6:9], v[2:3], off offset:512 nt
	s_nop 0
	global_load_dwordx4 v[2:5], v[2:3], off offset:576 nt
	s_mov_b32 s23, 0x20000
	s_mov_b64 s[30:31], 0x20000
	v_add_co_u32_e32 v146, vcc, s23, v158
	v_cvt_pk_bf16_f32 v142, v142, v143
	v_cvt_pk_bf16_f32 v143, v144, v145
	v_lshl_add_u64 v[144:145], v[158:159], 0, s[30:31]
	s_nop 0
	v_addc_co_u32_e32 v147, vcc, 0, v159, vcc
	s_waitcnt vmcnt(10)
	v_pk_fma_f32 v[138:139], v[138:139], v[20:21], v[192:193]
	s_waitcnt vmcnt(9)
	v_pk_fma_f32 v[134:135], v[134:135], v[24:25], v[196:197]
	s_waitcnt vmcnt(8)
	v_pk_fma_f32 v[132:133], v[132:133], v[26:27], v[202:203]
	v_pk_fma_f32 v[130:131], v[130:131], v[28:29], v[200:201]
	s_mov_b32 s23, 0xc0000
	global_store_dwordx2 v[146:147], v[142:143], off
	v_pk_fma_f32 v[140:141], v[140:141], v[18:19], v[194:195]
	v_cvt_pk_bf16_f32 v138, v138, v139
	v_pk_fma_f32 v[136:137], v[136:137], v[22:23], v[198:199]
	v_cvt_pk_bf16_f32 v139, v140, v141
	global_store_dwordx2 v[144:145], v[138:139], off offset:32
	v_cvt_pk_bf16_f32 v134, v134, v135
	v_cvt_pk_bf16_f32 v135, v136, v137
	global_store_dwordx2 v[144:145], v[134:135], off offset:256
	v_cvt_pk_bf16_f32 v130, v130, v131
	v_cvt_pk_bf16_f32 v131, v132, v133
	v_add_co_u32_e32 v132, vcc, s23, v174
	global_store_dwordx2 v[144:145], v[130:131], off offset:288
	s_mov_b64 s[30:31], 0xc0000
	v_addc_co_u32_e32 v133, vcc, 0, v175, vcc
	v_lshl_add_u64 v[130:131], v[174:175], 0, s[30:31]
	global_load_dwordx4 v[132:135], v[132:133], off nt
	s_nop 0
	global_load_dwordx4 v[136:139], v[130:131], off offset:64 nt
	global_load_dwordx4 v[140:143], v[130:131], off offset:512 nt
	global_load_dwordx4 v[144:147], v[130:131], off offset:576 nt
	s_mov_b32 s23, 0x200000
	s_mov_b64 s[30:31], 0x200000
	s_waitcnt vmcnt(11)
;     __device__ __forceinline__ void operator()(const f32x4 (&acc)[2][2][4][2], const Unit& u, int wr, int wc, int fr, int fq) const {
;     ...
;         ER_LOAD(B0, 0); ER_LOAD(B1, 1); ER_STORE(B0, 0); ER_LOAD(B0, 2); ER_STORE(B1, 1); ER_LOAD(B1, 3); ER_STORE(B0, 2); ER_LOAD(B0, 4); ER_STORE(B1, 3); ER_LOAD(B1, 5);
;         ER_STORE(B0, 4); ER_LOAD(B0, 6); ER_STORE(B1, 5); ER_LOAD(B1, 7); ER_STORE(B0, 6); ER_STORE(B1, 7);
	v_pk_fma_f32 v[16:17], v[128:129], v[30:31], v[16:17]
	v_pk_fma_f32 v[14:15], v[126:127], v[32:33], v[14:15]
	v_add_co_u32_e32 v126, vcc, s57, v158
	v_cvt_pk_bf16_f32 v14, v14, v15
	v_cvt_pk_bf16_f32 v15, v16, v17
	v_lshl_add_u64 v[16:17], v[158:159], 0, s[20:21]
	s_nop 0
	v_addc_co_u32_e32 v127, vcc, 0, v159, vcc
	s_waitcnt vmcnt(10)
	v_pk_fma_f32 v[10:11], v[122:123], v[20:21], v[10:11]
	s_waitcnt vmcnt(9)
	v_pk_fma_f32 v[6:7], v[118:119], v[24:25], v[6:7]
	s_waitcnt vmcnt(8)
	v_pk_fma_f32 v[4:5], v[116:117], v[26:27], v[4:5]
	v_pk_fma_f32 v[2:3], v[114:115], v[28:29], v[2:3]
	global_store_dwordx2 v[126:127], v[14:15], off
	v_pk_fma_f32 v[12:13], v[124:125], v[18:19], v[12:13]
	v_cvt_pk_bf16_f32 v10, v10, v11
	v_pk_fma_f32 v[8:9], v[120:121], v[22:23], v[8:9]
	v_cvt_pk_bf16_f32 v11, v12, v13
	global_store_dwordx2 v[16:17], v[10:11], off offset:32
	v_cvt_pk_bf16_f32 v6, v6, v7
	v_cvt_pk_bf16_f32 v7, v8, v9
	global_store_dwordx2 v[16:17], v[6:7], off offset:256
	v_cvt_pk_bf16_f32 v2, v2, v3
	v_cvt_pk_bf16_f32 v3, v4, v5
	v_add_co_u32_e32 v4, vcc, s23, v174
	global_store_dwordx2 v[16:17], v[2:3], off offset:288
	v_lshl_add_u64 v[2:3], v[174:175], 0, s[30:31]
	v_addc_co_u32_e32 v5, vcc, 0, v175, vcc
	global_load_dwordx4 v[14:17], v[4:5], off nt
	global_load_dwordx4 v[10:13], v[2:3], off offset:64 nt
	global_load_dwordx4 v[6:9], v[2:3], off offset:512 nt
	s_nop 0
	global_load_dwordx4 v[2:5], v[2:3], off offset:576 nt
	s_mov_b32 s23, 0x60000
	s_mov_b64 s[30:31], 0x60000
	s_waitcnt vmcnt(11)
	v_pk_fma_f32 v[112:113], v[112:113], v[30:31], v[134:135]
	v_pk_fma_f32 v[110:111], v[110:111], v[32:33], v[132:133]
	v_add_co_u32_e32 v114, vcc, s23, v158
	v_cvt_pk_bf16_f32 v110, v110, v111
	v_cvt_pk_bf16_f32 v111, v112, v113
	v_lshl_add_u64 v[112:113], v[158:159], 0, s[30:31]
	s_nop 0
	v_addc_co_u32_e32 v115, vcc, 0, v159, vcc
	s_waitcnt vmcnt(10)
	v_pk_fma_f32 v[106:107], v[106:107], v[20:21], v[136:137]
	s_waitcnt vmcnt(9)
	v_pk_fma_f32 v[102:103], v[102:103], v[24:25], v[140:141]
	s_waitcnt vmcnt(8)
	v_pk_fma_f32 v[100:101], v[100:101], v[26:27], v[146:147]
	v_pk_fma_f32 v[98:99], v[98:99], v[28:29], v[144:145]
	s_mov_b32 s23, 0x240000
	global_store_dwordx2 v[114:115], v[110:111], off
	v_pk_fma_f32 v[108:109], v[108:109], v[18:19], v[138:139]
	v_cvt_pk_bf16_f32 v106, v106, v107
	v_pk_fma_f32 v[104:105], v[104:105], v[22:23], v[142:143]
	v_cvt_pk_bf16_f32 v107, v108, v109
	global_store_dwordx2 v[112:113], v[106:107], off offset:32
	v_cvt_pk_bf16_f32 v102, v102, v103
	v_cvt_pk_bf16_f32 v103, v104, v105
	global_store_dwordx2 v[112:113], v[102:103], off offset:256
	v_cvt_pk_bf16_f32 v98, v98, v99
	v_cvt_pk_bf16_f32 v99, v100, v101
	v_add_co_u32_e32 v100, vcc, s23, v174
	global_store_dwordx2 v[112:113], v[98:99], off offset:288
	s_mov_b64 s[30:31], 0x240000
	v_addc_co_u32_e32 v101, vcc, 0, v175, vcc
	v_lshl_add_u64 v[98:99], v[174:175], 0, s[30:31]
	global_load_dwordx4 v[100:103], v[100:101], off nt
	s_nop 0
	global_load_dwordx4 v[104:107], v[98:99], off offset:64 nt
	global_load_dwordx4 v[108:111], v[98:99], off offset:512 nt
	global_load_dwordx4 v[112:115], v[98:99], off offset:576 nt
	s_mov_b32 s23, 0x100000
	s_mov_b64 s[30:31], 0x100000
	s_waitcnt vmcnt(11)
	v_pk_fma_f32 v[16:17], v[96:97], v[30:31], v[16:17]
	v_pk_fma_f32 v[14:15], v[94:95], v[32:33], v[14:15]
	v_add_co_u32_e32 v94, vcc, s23, v158
	v_cvt_pk_bf16_f32 v14, v14, v15
	v_cvt_pk_bf16_f32 v15, v16, v17
	v_lshl_add_u64 v[16:17], v[158:159], 0, s[30:31]
	s_nop 0
	v_addc_co_u32_e32 v95, vcc, 0, v159, vcc
	s_waitcnt vmcnt(10)
	v_pk_fma_f32 v[10:11], v[90:91], v[20:21], v[10:11]
	s_waitcnt vmcnt(9)
	v_pk_fma_f32 v[6:7], v[86:87], v[24:25], v[6:7]
	s_waitcnt vmcnt(8)
	v_pk_fma_f32 v[4:5], v[84:85], v[26:27], v[4:5]
	v_pk_fma_f32 v[2:3], v[82:83], v[28:29], v[2:3]
	s_mov_b32 s23, 0x280000
	global_store_dwordx2 v[94:95], v[14:15], off
	v_pk_fma_f32 v[12:13], v[92:93], v[18:19], v[12:13]
	v_cvt_pk_bf16_f32 v10, v10, v11
	v_pk_fma_f32 v[8:9], v[88:89], v[22:23], v[8:9]
	v_cvt_pk_bf16_f32 v11, v12, v13
	global_store_dwordx2 v[16:17], v[10:11], off offset:32
	v_cvt_pk_bf16_f32 v6, v6, v7
	v_cvt_pk_bf16_f32 v7, v8, v9
	global_store_dwordx2 v[16:17], v[6:7], off offset:256
	v_cvt_pk_bf16_f32 v2, v2, v3
	v_cvt_pk_bf16_f32 v3, v4, v5
	s_mov_b64 s[30:31], 0x280000
	v_add_co_u32_e32 v4, vcc, s23, v174
	global_store_dwordx2 v[16:17], v[2:3], off offset:288
	v_lshl_add_u64 v[2:3], v[174:175], 0, s[30:31]
	v_addc_co_u32_e32 v5, vcc, 0, v175, vcc
	global_load_dwordx4 v[14:17], v[4:5], off nt
	global_load_dwordx4 v[10:13], v[2:3], off offset:64 nt
	global_load_dwordx4 v[6:9], v[2:3], off offset:512 nt
	s_nop 0
	global_load_dwordx4 v[2:5], v[2:3], off offset:576 nt
	s_mov_b32 s23, 0x120000
	s_mov_b64 s[30:31], 0x120000
	s_waitcnt vmcnt(11)
; #define PG8_BAR __builtin_amdgcn_s_barrier()
;     ...
;         if (!has_next) break;
; #pragma unroll
;         for (int a = 0; a < 2; ++a)
; #pragma unroll
;             for (int b = 0; b < 2; ++b)
; #pragma unroll
;                 for (int m = 0; m < 4; ++m)
; #pragma unroll
;                     for (int n = 0; n < 2; ++n) acc[a][b][m][n] = (f32x4){0.f, 0.f, 0.f, 0.f};
;         cur = nxt; cA = nA; cB = nB; ++ui;
;         if constexpr (ALIGN_EPI) { if (wr == 1) PG8_BAR; }
;     __device__ __forceinline__ void operator()(const f32x4 (&acc)[2][2][4][2], const Unit& u, int wr, int wc, int fr, int fq) const {
;     ...
;         ER_LOAD(B0, 0); ER_LOAD(B1, 1); ER_STORE(B0, 0); ER_LOAD(B0, 2); ER_STORE(B1, 1); ER_LOAD(B1, 3); ER_STORE(B0, 2); ER_LOAD(B0, 4); ER_STORE(B1, 3); ER_LOAD(B1, 5);
;         ER_STORE(B0, 4); ER_LOAD(B0, 6); ER_STORE(B1, 5); ER_LOAD(B1, 7); ER_STORE(B0, 6); ER_STORE(B1, 7);
	v_pk_fma_f32 v[80:81], v[80:81], v[30:31], v[102:103]
	v_pk_fma_f32 v[78:79], v[78:79], v[32:33], v[100:101]
	v_add_co_u32_e32 v82, vcc, s23, v158
	v_cvt_pk_bf16_f32 v78, v78, v79
	v_cvt_pk_bf16_f32 v79, v80, v81
	v_lshl_add_u64 v[80:81], v[158:159], 0, s[30:31]
	s_nop 0
	v_addc_co_u32_e32 v83, vcc, 0, v159, vcc
	s_waitcnt vmcnt(10)
	v_pk_fma_f32 v[74:75], v[74:75], v[20:21], v[104:105]
	s_waitcnt vmcnt(9)
	v_pk_fma_f32 v[70:71], v[70:71], v[24:25], v[108:109]
	s_waitcnt vmcnt(8)
	v_pk_fma_f32 v[68:69], v[68:69], v[26:27], v[114:115]
	v_pk_fma_f32 v[66:67], v[66:67], v[28:29], v[112:113]
	s_mov_b32 s23, 0x2c0000
	global_store_dwordx2 v[82:83], v[78:79], off
	v_pk_fma_f32 v[76:77], v[76:77], v[18:19], v[106:107]
	v_cvt_pk_bf16_f32 v74, v74, v75
	v_pk_fma_f32 v[72:73], v[72:73], v[22:23], v[110:111]
	v_cvt_pk_bf16_f32 v75, v76, v77
	global_store_dwordx2 v[80:81], v[74:75], off offset:32
	v_cvt_pk_bf16_f32 v70, v70, v71
	v_cvt_pk_bf16_f32 v71, v72, v73
	global_store_dwordx2 v[80:81], v[70:71], off offset:256
	v_cvt_pk_bf16_f32 v66, v66, v67
	v_cvt_pk_bf16_f32 v67, v68, v69
	v_add_co_u32_e32 v68, vcc, s23, v174
	global_store_dwordx2 v[80:81], v[66:67], off offset:288
	s_mov_b64 s[30:31], 0x2c0000
	v_addc_co_u32_e32 v69, vcc, 0, v175, vcc
	v_lshl_add_u64 v[66:67], v[174:175], 0, s[30:31]
	global_load_dwordx4 v[68:71], v[68:69], off nt
	s_nop 0
	global_load_dwordx4 v[72:75], v[66:67], off offset:64 nt
	global_load_dwordx4 v[76:79], v[66:67], off offset:512 nt
	global_load_dwordx4 v[80:83], v[66:67], off offset:576 nt
	s_mov_b32 s23, 0x140000
	s_mov_b64 s[30:31], 0x140000
	s_waitcnt vmcnt(11)
	v_pk_fma_f32 v[16:17], v[64:65], v[30:31], v[16:17]
	v_pk_fma_f32 v[14:15], v[62:63], v[32:33], v[14:15]
	v_add_co_u32_e32 v62, vcc, s23, v158
	v_cvt_pk_bf16_f32 v14, v14, v15
	v_cvt_pk_bf16_f32 v15, v16, v17
	v_lshl_add_u64 v[16:17], v[158:159], 0, s[30:31]
	s_nop 0
	v_addc_co_u32_e32 v63, vcc, 0, v159, vcc
	s_waitcnt vmcnt(10)
	v_pk_fma_f32 v[10:11], v[58:59], v[20:21], v[10:11]
	s_waitcnt vmcnt(9)
	v_pk_fma_f32 v[6:7], v[50:51], v[24:25], v[6:7]
	global_store_dwordx2 v[62:63], v[14:15], off
	v_pk_fma_f32 v[12:13], v[60:61], v[18:19], v[12:13]
	v_cvt_pk_bf16_f32 v10, v10, v11
	s_mov_b32 s23, 0x160000
	v_cvt_pk_bf16_f32 v11, v12, v13
	global_store_dwordx2 v[16:17], v[10:11], off offset:32
	v_cvt_pk_bf16_f32 v6, v6, v7
	v_pk_fma_f32 v[8:9], v[52:53], v[22:23], v[8:9]
	s_waitcnt vmcnt(10)
	v_pk_fma_f32 v[4:5], v[48:49], v[26:27], v[4:5]
	v_cvt_pk_bf16_f32 v7, v8, v9
	global_store_dwordx2 v[16:17], v[6:7], off offset:256
	v_pk_fma_f32 v[2:3], v[46:47], v[28:29], v[2:3]
	v_add_co_u32_e32 v6, vcc, s23, v158
	v_cvt_pk_bf16_f32 v2, v2, v3
	v_cvt_pk_bf16_f32 v3, v4, v5
	global_store_dwordx2 v[16:17], v[2:3], off offset:288
	s_nop 0
	v_addc_co_u32_e32 v7, vcc, 0, v159, vcc
	s_mov_b64 s[30:31], 0x160000
	s_andn2_b64 vcc, exec, s[2:3]
	s_waitcnt vmcnt(7)
	v_pk_fma_f32 v[4:5], v[54:55], v[32:33], v[68:69]
	v_pk_fma_f32 v[2:3], v[56:57], v[30:31], v[70:71]
	v_cvt_pk_bf16_f32 v4, v4, v5
	s_nop 0
	v_cvt_pk_bf16_f32 v5, v2, v3
	global_store_dwordx2 v[6:7], v[4:5], off
	s_waitcnt vmcnt(7)
	v_pk_fma_f32 v[6:7], v[42:43], v[20:21], v[72:73]
	v_lshl_add_u64 v[2:3], v[158:159], 0, s[30:31]
	v_pk_fma_f32 v[4:5], v[44:45], v[18:19], v[74:75]
	v_cvt_pk_bf16_f32 v6, v6, v7
	s_mov_b64 s[30:31], -1
	v_cvt_pk_bf16_f32 v7, v4, v5
	global_store_dwordx2 v[2:3], v[6:7], off offset:32
	s_waitcnt vmcnt(7)
	v_pk_fma_f32 v[6:7], v[38:39], v[24:25], v[76:77]
	v_pk_fma_f32 v[4:5], v[40:41], v[22:23], v[78:79]
	v_cvt_pk_bf16_f32 v6, v6, v7
	s_nop 0
	v_cvt_pk_bf16_f32 v7, v4, v5
	global_store_dwordx2 v[2:3], v[6:7], off offset:256
	s_waitcnt vmcnt(7)
	v_pk_fma_f32 v[6:7], v[34:35], v[28:29], v[80:81]
	v_pk_fma_f32 v[4:5], v[36:37], v[26:27], v[82:83]
	v_cvt_pk_bf16_f32 v6, v6, v7
	s_nop 0
	v_cvt_pk_bf16_f32 v7, v4, v5
	global_store_dwordx2 v[2:3], v[6:7], off offset:288
	s_cbranch_vccnz .LBB0_2074
	s_andn2_b64 vcc, exec, s[0:1]
	s_cbranch_vccnz .LBB0_2073
	s_barrier
	s_branch .LBB0_2073
